# grid barrier wait keeps two polls of the arrival counter in flight (half a round trip apart) instead of one
# speedup vs baseline: 1.0135x; 1.0020x over previous
.Lxb_poll_0:
	s_mov_b32 s8, 0
	global_load_dword v2, v87, s[6:7] sc1
	s_sleep 24
.Lxb_spin_0:
	global_load_dword v4, v87, s[6:7] sc1
	s_waitcnt vmcnt(1)
	v_cmp_le_u32_e32 vcc, v5, v2
	s_cbranch_vccnz .Lxb_done_0
	global_load_dword v2, v87, s[6:7] sc1
	s_waitcnt vmcnt(1)
	v_cmp_le_u32_e32 vcc, v5, v4
	s_cbranch_vccnz .Lxb_done_0
	s_add_i32 s8, s8, 1
	s_cmpk_lt_u32 s8, 0x2000
	s_cbranch_scc1 .Lxb_spin_0
